# four critical-path trims (hgrn_out2 counted wait, rescale test before the tile barrier, gate/up token-map loads batched, kv2 value-row loads batched) with 4-byte pads so every hot loop keeps the byte
# speedup vs baseline: 1.0015x; 1.0015x over previous
; __device__ __forceinline__ unsigned cvtpk(float lo, float hi) { unsigned r; asm volatile("v_cvt_pk_bf16_f32 %0, %1, %2" : "=v"(r) : "v"(lo), "v"(hi)); return r; }
; __device__ __forceinline__ int v_st(int k, int c) { const int kk = (k & ~0xC) | ((k & 4) << 1) | ((k & 8) >> 1); return ((kk >> 3) * 4 + (c >> 5)) * 512 + ((kk & 7) * 32 + (c & 31)) * 2; }
; __device__ __forceinline__ int v_rd_base(int lane) { return ((lane & 3) << 3) | (((lane >> 2) & 3) << 6) | (((lane >> 4) & 1) << 5) | (((lane >> 5) & 1) << 8); }
; #define SWRITE(b, i) do { *(LAS bf16x8*)(V_lds + (b) * SHM_V + vst0) = sr_[i].vs0;          \
;     *(LAS bf16x8*)(V_lds + (b) * SHM_V + vst1) = sr_[i].vs1; int kc = sc * 2;               \
;     *(LAS bf16x8*)(K_lds + (b) * SHM_K + KSWZ(sr, kc)) = sr_[i].ks0;                       \
;     *(LAS bf16x8*)(K_lds + (b) * SHM_K + KSWZ(32 + sr, kc)) = sr_[i].ks1; } while (0)
; #define SWAIT() asm volatile("s_waitcnt vmcnt(4)" ::: "memory")
; template <bool HALF> __device__ __forceinline__ void dense_body(const bf16_t* __restrict__ Qb, const bf16_t* __restrict__ Kh, const bf16_t* __restrict__ Vh, ...
;     ...
;     for (int d0 = 0; d0 < NQ; ++d0) { u32x4 w;
; #pragma unroll
;       for (int j = 0; j < 4; ++j) w[j] = cvtpk(qf[d0][2 * j], qf[d0][2 * j + 1]);
;       qr[d0] = *reinterpret_cast<bf16x8*>(&w); } }
;   const int sr = tid >> 4, sc = (tid & 15) * 8, vst0 = v_st(sr, sc), vst1 = v_st(32 + sr, sc);
;   const int vb0 = (int)(uintptr_t)V_lds + v_rd_base(lane);
;   struct { bf16x8 vs0, vs1, ks0, ks1; } sr_[2];
;   const unsigned ko0 = (unsigned)(sr * LDKK + sc) * 2u, ko1 = ko0 + 32u * LDKK * 2u, vo0 = (unsigned)(sr * LDKV + sc) * 2u, vo1 = vo0 + 32u * LDKV * 2u;
;     ...
;   f32x16 pA0, pA1, pB0, pB1; float mnA, mnB, alA, alB; bf16x8 pa0, pa1, pa2, pa3; const int NT = seq / KVBLK;
;   const char* Kl0 = (const char*)K_lds; const char* Kl1 = (const char*)(K_lds + SHM_K);
;   constexpr int SE = 0, SO = 1;
;   SLOAD(SE, 0); asm volatile("s_waitcnt vmcnt(0)" ::: "memory"); SWRITE(0, SE); __syncthreads();
;   qkt<HALF>(pA0, pA1, Kl0, qr, r32, hi, koff); partialSM(pA0, pA1, m_reg, mnA, alA);
;   SLOAD(SO, KVBLK); if (2 < NT) SLOAD(SE, 2 * KVBLK);
;   SWAIT(); SWRITE(1, SO); __syncthreads();
.LBB0_424:
	s_ashr_i32 s6, s2, 2
	s_add_i32 s2, s2, -8
	s_lshr_b32 s2, s2, 1
	s_add_i32 s7, s2, 2
	s_and_b64 s[2:3], s[20:21], exec
	s_cselect_b32 s3, s6, s7
	s_lshl_b32 s2, s3, 7
	s_cmp_lt_i32 s3, 2
	s_movk_i32 s3, 0x1100
	s_cselect_b32 s3, s3, 0x1500
	s_add_i32 s6, s3, s2
	s_ashr_i32 s3, s2, 31
	s_lshl_b64 s[20:21], s[2:3], 1
	s_add_u32 s34, s44, s20
	v_cvt_pk_bf16_f32 v118, v122, v36
	v_cvt_pk_bf16_f32 v119, v123, v37
	v_cvt_pk_bf16_f32 v120, v120, v28
	v_cvt_pk_bf16_f32 v121, v121, v29
	v_cvt_pk_bf16_f32 v126, v114, v32
	v_cvt_pk_bf16_f32 v127, v115, v33
	v_cvt_pk_bf16_f32 v128, v112, v24
	v_cvt_pk_bf16_f32 v129, v113, v25
	v_cvt_pk_bf16_f32 v122, v108, v26
	v_cvt_pk_bf16_f32 v123, v109, v27
	v_cvt_pk_bf16_f32 v124, v106, v20
	v_cvt_pk_bf16_f32 v125, v107, v21
	v_cvt_pk_bf16_f32 v114, v104, v22
	v_cvt_pk_bf16_f32 v115, v105, v23
	v_cvt_pk_bf16_f32 v116, v74, v16
	v_cvt_pk_bf16_f32 v117, v75, v17
	v_ashrrev_i32_e32 v16, 4, v142
	v_lshlrev_b32_e32 v17, 3, v142
	s_movk_i32 s2, 0x300
	s_addc_u32 s35, s45, s21
	s_ashr_i32 s7, s6, 31
	v_cvt_pk_bf16_f32 v110, v72, v18
	v_and_b32_e32 v18, 0x78, v17
	v_mul_lo_u32 v0, v16, s2
	s_movk_i32 s2, 0x1800
	s_lshl_b64 s[22:23], s[6:7], 1
	v_cvt_pk_bf16_f32 v111, v73, v19
	v_cvt_pk_bf16_f32 v112, v70, v12
	v_cvt_pk_bf16_f32 v113, v71, v13
	v_cvt_pk_bf16_f32 v106, v68, v14
	v_cvt_pk_bf16_f32 v107, v69, v15
	v_cvt_pk_bf16_f32 v108, v6, v8
	v_or_b32_e32 v8, v0, v18
	v_mul_lo_u32 v0, v16, s2
	s_add_u32 s38, s30, s22
	v_or_b32_e32 v0, v0, v18
	s_addc_u32 s39, s31, s23
	v_lshlrev_b32_e32 v50, 1, v0
	v_cvt_pk_bf16_f32 v109, v7, v9
	v_cvt_pk_bf16_f32 v102, v4, v10
	v_cvt_pk_bf16_f32 v103, v5, v11
	v_cvt_pk_bf16_f32 v104, v2, v64
	v_cvt_pk_bf16_f32 v105, v1, v65
	v_cvt_pk_bf16_f32 v98, v40, v46
	v_cvt_pk_bf16_f32 v99, v39, v47
	v_cvt_pk_bf16_f32 v100, v34, v42
	v_cvt_pk_bf16_f32 v101, v31, v43
	v_add_u32_e32 v48, 0x60000, v50
	v_readlane_b32 s52, v252, 4
	s_nop 3
	v_and_b32_e32 v134, 63, v142
	v_lshrrev_b32_e32 v135, 4, v134
	v_and_b32_e32 v136, 15, v134
	s_lshl_b32 s53, s52, 3
	v_add_u32_e32 v137, s53, v135
	v_xor_b32_e32 v138, v136, v135
	v_mul_u32_u24_e32 v130, 0x600, v137
	v_lshl_add_u32 v130, v138, 4, v130
	v_add_u32_e32 v139, 4, v135
	v_xor_b32_e32 v138, v136, v139
	v_add_u32_e32 v137, 4, v137
	v_mul_u32_u24_e32 v131, 0x600, v137
	v_lshl_add_u32 v131, v138, 4, v131
	v_bfe_u32 v135, v134, 2, 3
	v_add_u32_e32 v135, s53, v135
	v_and_b32_e32 v136, 4, v135
	v_and_b32_e32 v137, 8, v135
	v_and_b32_e32 v135, 0xfffffff3, v135
	v_lshl_or_b32 v135, v136, 1, v135
	v_lshrrev_b32_e32 v137, 1, v137
	v_or_b32_e32 v135, v135, v137
	v_mul_u32_u24_e32 v132, 0x3000, v135
	v_lshrrev_b32_e32 v136, 5, v134
	v_lshl_add_u32 v132, v136, 6, v132
	v_and_b32_e32 v136, 3, v134
	v_lshl_add_u32 v132, v136, 4, v132
	v_add_u32_e32 v133, 0x80, v132
	v_mov_b32_e32 v140, v132
	v_mov_b32_e32 v141, v133
	s_lshl_b32 s53, s52, 11
	s_add_i32 s52, s53, 0x8000
	s_add_i32 m0, s52, 0x0
	s_nop 0
	global_load_lds_dwordx4 v130, s[34:35]
	s_add_i32 m0, s52, 0x400
	s_nop 0
	global_load_lds_dwordx4 v131, s[34:35]
	s_add_i32 m0, s53, 0x0
	s_nop 0
	global_load_lds_dwordx4 v132, s[38:39]
	s_add_i32 m0, s53, 0x400
	s_nop 0
	global_load_lds_dwordx4 v133, s[38:39]
	s_add_u32 s48, s34, 0x18000
	s_addc_u32 s49, s35, 0
	s_add_u32 s50, s38, 0xc0000
	s_addc_u32 s51, s39, 0
	s_add_i32 m0, s52, 0x4000
	s_nop 0
	global_load_lds_dwordx4 v130, s[48:49]
	s_add_i32 m0, s52, 0x4400
	s_nop 0
	global_load_lds_dwordx4 v131, s[48:49]
	s_add_i32 m0, s53, 0x4000
	s_nop 0
	global_load_lds_dwordx4 v132, s[50:51]
	s_add_i32 m0, s53, 0x4400
	s_nop 0
	global_load_lds_dwordx4 v133, s[50:51]
	s_add_u32 s48, s48, 0x18000
	s_addc_u32 s49, s49, 0
	s_add_u32 s50, s50, 0xc0000
	s_addc_u32 s51, s51, 0
	v_lshlrev_b32_e32 v52, 1, v8
	v_add_u32_e32 v54, 0xc000, v52
	v_and_b32_e32 v20, 0xfffff0, v16
	v_lshlrev_b32_e32 v21, 1, v16
	v_lshrrev_b32_e32 v22, 1, v16
	v_and_b32_e32 v23, 3, v16
	v_add_u32_e32 v24, 32, v16
	v_and_or_b32 v20, v21, 8, v20
	v_and_or_b32 v21, v22, 4, v23
	v_and_b32_e32 v22, 0xfffff0, v24
	v_lshlrev_b32_e32 v23, 1, v24
	v_bfe_u32 v17, v17, 5, 2
	v_lshrrev_b32_e32 v20, 1, v20
	v_and_or_b32 v22, v23, 8, v22
	v_lshlrev_b32_e32 v18, 1, v18
	v_or_b32_e32 v20, v20, v17
	v_lshrrev_b32_e32 v22, 1, v22
	v_lshlrev_b32_e32 v21, 6, v21
	v_and_b32_e32 v25, 48, v18
	v_lshlrev_b32_e32 v20, 9, v20
	v_or_b32_e32 v17, v22, v17
	v_or3_b32 v20, v20, v21, v25
	v_lshlrev_b32_e32 v17, 9, v17
	v_or3_b32 v17, v17, v21, v25
	v_add_u32_e32 v205, 0, v20
	v_and_b32_e32 v19, 0x70, v142
	v_lshlrev_b32_e32 v16, 8, v16
	v_add_u32_e32 v206, 0, v17
	s_waitcnt vmcnt(0)
	v_bitop3_b32 v16, v18, v16, v19 bitop3:0xde
	v_lshlrev_b32_e32 v0, 8, v24
	v_bitop3_b32 v0, v18, v0, v19 bitop3:0xde
	v_add_u32_e32 v207, 0, v16
	v_add_u32_e32 v208, 0, v0
	v_lshlrev_b32_e32 v0, 4, v197
	v_lshlrev_b32_e32 v8, 8, v197
	v_and_b32_e32 v9, 0x70, v0
	v_bitop3_b32 v0, v96, v8, v9 bitop3:0xde
	v_add_u32_e32 v209, 0, v0
	s_waitcnt lgkmcnt(0)
	s_barrier
; #define SWRITE(b, i) do { *(LAS bf16x8*)(V_lds + (b) * SHM_V + vst0) = sr_[i].vs0;          \
;     *(LAS bf16x8*)(V_lds + (b) * SHM_V + vst1) = sr_[i].vs1; int kc = sc * 2;               \
;     *(LAS bf16x8*)(K_lds + (b) * SHM_K + KSWZ(sr, kc)) = sr_[i].ks0;                       \
;     *(LAS bf16x8*)(K_lds + (b) * SHM_K + KSWZ(32 + sr, kc)) = sr_[i].ks1; } while (0)
; template <bool HALF> __device__ __forceinline__ void qkt(f32x16& p0, f32x16& p1, const char* Ks, const bf16x8* qr, int r32, int hi, int koff) {
;   p0 = f32x16{}; p1 = f32x16{};
;   for (int d0 = 0; d0 < (HALF ? 4 : 8); ++d0) { int cb = (d0 * 16 + hi * 8) * 2 + koff;
;     bf16x8 b0 = *reinterpret_cast<const bf16x8*>(Ks + KSWZ(r32, cb));
;     bf16x8 b1 = *reinterpret_cast<const bf16x8*>(Ks + KSWZ(32 + r32, cb));
;     p0 = __builtin_amdgcn_mfma_f32_32x32x16_bf16(b0, qr[d0], p0, 0, 0, 0);
;     p1 = __builtin_amdgcn_mfma_f32_32x32x16_bf16(b1, qr[d0], p1, 0, 0, 0); }
; template <bool HALF> __device__ __forceinline__ void dense_body(const bf16_t* __restrict__ Qb, const bf16_t* __restrict__ Kh, const bf16_t* __restrict__ Vh, ...
;     ...
;   SLOAD(SE, 0); asm volatile("s_waitcnt vmcnt(0)" ::: "memory"); SWRITE(0, SE); __syncthreads();
;   qkt<HALF>(pA0, pA1, Kl0, qr, r32, hi, koff); partialSM(pA0, pA1, m_reg, mnA, alA);
	ds_read_b128 v[0:3], v209 offset:32768
	ds_read_b128 v[4:7], v209 offset:40960
	s_waitcnt lgkmcnt(1)
	v_mfma_f32_32x32x16_bf16 v[16:31], v[0:3], v[118:121], 0
	v_or_b32_e32 v0, 32, v96
	v_bitop3_b32 v0, v0, v8, v9 bitop3:0xde
	v_add_u32_e32 v221, 0, v0
	v_and_b32_e32 v76, 63, v142
	v_and_b32_e32 v10, 0x3fffffc0, v142
	s_add_i32 s46, 0, 0x10000
	v_lshl_add_u32 v200, v10, 2, s46
	s_waitcnt lgkmcnt(0)
	v_mfma_f32_32x32x16_bf16 v[32:47], v[4:7], v[118:121], 0
	ds_read_b128 v[0:3], v221 offset:32768
	ds_read_b128 v[4:7], v221 offset:40960
	v_lshlrev_b32_e32 v10, 3, v76
	s_add_u32 s6, s34, 0x18000
	s_addc_u32 s7, s35, 0
	s_add_u32 s16, s38, 0xc0000
	s_addc_u32 s17, s39, 0
	s_mov_b32 s64, s65
	s_waitcnt lgkmcnt(1)
	v_mfma_f32_32x32x16_bf16 v[16:31], v[0:3], v[126:129], v[16:31]
	v_or_b32_e32 v0, 64, v96
	v_bitop3_b32 v0, v0, v8, v9 bitop3:0xde
	v_add_u32_e32 v222, 0, v0
	s_mov_b32 s66, s65
	s_mov_b32 s67, s65
	s_mov_b32 s68, s65
	s_mov_b32 s69, s65
	s_waitcnt lgkmcnt(0)
	v_mfma_f32_32x32x16_bf16 v[32:47], v[4:7], v[126:129], v[32:47]
	ds_read_b128 v[0:3], v222 offset:32768
	ds_read_b128 v[4:7], v222 offset:40960
	s_mov_b32 s70, s65
	s_mov_b32 s71, s65
	s_mov_b32 s72, s65
	s_mov_b32 s73, s65
	s_mov_b32 s74, s65
	s_mov_b32 s75, s65
	s_waitcnt lgkmcnt(1)
	v_mfma_f32_32x32x16_bf16 v[16:31], v[0:3], v[122:125], v[16:31]
	v_or_b32_e32 v0, 0x60, v96
	v_bitop3_b32 v0, v0, v8, v9 bitop3:0xde
	v_add_u32_e32 v210, 0, v0
	s_mov_b32 s76, s65
	s_mov_b32 s77, s65
	s_mov_b32 s78, s65
	s_mov_b32 s79, s65
	s_waitcnt lgkmcnt(0)
	v_mfma_f32_32x32x16_bf16 v[32:47], v[4:7], v[122:125], v[32:47]
	ds_read_b128 v[0:3], v210 offset:32768
	ds_read_b128 v[4:7], v210 offset:40960
	v_mov_b32_e32 v51, v97
	v_mov_b32_e32 v49, v97
	v_mov_b32_e32 v53, v97
	v_mov_b32_e32 v55, v97
	v_lshl_add_u64 v[180:181], s[22:23], 0, v[50:51]
	v_lshl_add_u64 v[182:183], s[22:23], 0, v[48:49]
	s_waitcnt lgkmcnt(1)
	v_mfma_f32_32x32x16_bf16 v[16:31], v[0:3], v[114:117], v[16:31]
	v_or_b32_e32 v0, 0x80, v96
	v_bitop3_b32 v0, v0, v8, v9 bitop3:0xde
	v_add_u32_e32 v211, 0, v0
	ds_read_b128 v[0:3], v211 offset:32768
	v_lshl_add_u64 v[184:185], s[20:21], 0, v[52:53]
	v_lshl_add_u64 v[186:187], s[20:21], 0, v[54:55]
	s_mov_b32 s2, 4
	s_waitcnt lgkmcnt(1)
	v_mfma_f32_32x32x16_bf16 v[32:47], v[4:7], v[114:117], v[32:47]
	ds_read_b128 v[4:7], v211 offset:40960
	v_cmp_gt_u32_e64 s[40:41], 32, v76
	v_lshl_add_u32 v201, v197, 2, v200
	v_mov_b32_e32 v202, 0
	s_waitcnt lgkmcnt(1)
	v_mfma_f32_32x32x16_bf16 v[16:31], v[0:3], v[110:113], v[16:31]
	v_lshlrev_b32_e32 v0, 4, v76
	v_and_b32_e32 v0, 0xc0, v0
	v_and_or_b32 v11, v10, 24, v0
	v_or_b32_e32 v0, 0xa0, v96
	v_bitop3_b32 v0, v0, v8, v9 bitop3:0xde
	v_add_u32_e32 v223, 0, v0
	v_and_b32_e32 v10, 0x100, v10
	s_waitcnt lgkmcnt(0)
	v_mfma_f32_32x32x16_bf16 v[32:47], v[4:7], v[110:113], v[32:47]
	ds_read_b128 v[0:3], v223 offset:32768
	ds_read_b128 v[4:7], v223 offset:40960
	s_add_u32 s6, s34, 0x30000
	s_addc_u32 s7, s35, 0
	s_waitcnt lgkmcnt(1)
	v_mfma_f32_32x32x16_bf16 v[16:31], v[0:3], v[106:109], v[16:31]
	v_lshlrev_b32_e32 v0, 1, v76
	v_and_b32_e32 v12, 32, v0
	v_or_b32_e32 v0, 0xc0, v96
	v_bitop3_b32 v0, v0, v8, v9 bitop3:0xde
	v_add_u32_e32 v225, 0, v0
	ds_read_b128 v[0:3], v225 offset:32768
	v_or3_b32 v77, v11, v12, v10
	s_waitcnt lgkmcnt(1)
	v_mfma_f32_32x32x16_bf16 v[32:47], v[4:7], v[106:109], v[32:47]
	ds_read_b128 v[4:7], v225 offset:40960
	v_add_u32_e32 v204, 0, v77
	s_waitcnt lgkmcnt(1)
	v_mfma_f32_32x32x16_bf16 v[16:31], v[0:3], v[102:105], v[16:31]
	v_or_b32_e32 v0, 0xe0, v96
	v_bitop3_b32 v0, v0, v8, v9 bitop3:0xde
	v_add_u32_e32 v224, 0, v0
	ds_read_b128 v[0:3], v224 offset:32768
	ds_read_b128 v[72:75], v224 offset:40960
	s_add_u32 s6, s38, 0x180000
	s_addc_u32 s7, s39, 0
	s_waitcnt lgkmcnt(2)
	v_mfma_f32_32x32x16_bf16 v[32:47], v[4:7], v[102:105], v[32:47]
	s_waitcnt lgkmcnt(1)
	v_mfma_f32_32x32x16_bf16 v[16:31], v[0:3], v[98:101], v[16:31]
	v_mov_b64_e32 v[0:1], s[64:65]
	v_mov_b64_e32 v[14:15], s[78:79]
	v_mov_b64_e32 v[2:3], s[66:67]
	v_mov_b64_e32 v[4:5], s[68:69]
	v_mov_b64_e32 v[6:7], s[70:71]
	v_mov_b64_e32 v[8:9], s[72:73]
	v_mov_b64_e32 v[10:11], s[74:75]
	s_waitcnt lgkmcnt(0)
; #define SWRITE(b, i) do { *(LAS bf16x8*)(V_lds + (b) * SHM_V + vst0) = sr_[i].vs0;          \
;     *(LAS bf16x8*)(V_lds + (b) * SHM_V + vst1) = sr_[i].vs1; int kc = sc * 2;               \
;     *(LAS bf16x8*)(K_lds + (b) * SHM_K + KSWZ(sr, kc)) = sr_[i].ks0;                       \
;     *(LAS bf16x8*)(K_lds + (b) * SHM_K + KSWZ(32 + sr, kc)) = sr_[i].ks1; } while (0)
; #define SWAIT() asm volatile("s_waitcnt vmcnt(4)" ::: "memory")
; __device__ __forceinline__ void partialSM(f32x16& p0, f32x16& p1, float& m_reg, float& mn, float& alpha) {
;   constexpr float C = SCALE * 1.4426950408889634f;
;   float pmax = p0[0]; for (int r = 1; r < 16; ++r) pmax = fmaxf(pmax, p0[r]); for (int r = 0; r < 16; ++r) pmax = fmaxf(pmax, p1[r]);
;   { auto rr = __builtin_amdgcn_permlane32_swap(__float_as_uint(pmax), __float_as_uint(pmax), false, false);
;     pmax = fmaxf(__uint_as_float(rr[0]), __uint_as_float(rr[1])); }
;   if (__builtin_expect(__all(pmax - m_reg <= THR / SCALE), 1)) { mn = m_reg; alpha = 1.f; }
;   else { mn = fmaxf(m_reg, pmax); alpha = __builtin_amdgcn_exp2f((m_reg - mn) * C); m_reg = mn; }
;   float mnC = -mn * C;
;   for (int r = 0; r < 16; ++r) p0[r] = fmaf(p0[r], C, mnC); for (int r = 0; r < 16; ++r) p1[r] = fmaf(p1[r], C, mnC);
;   for (int r = 0; r < 16; ++r) p0[r] = __builtin_amdgcn_exp2f(p0[r]);
; }
; template <bool HALF> __device__ __forceinline__ void dense_body(const bf16_t* __restrict__ Qb, const bf16_t* __restrict__ Kh, const bf16_t* __restrict__ Vh, ...
;     ...
;   SLOAD(SO, KVBLK); if (2 < NT) SLOAD(SE, 2 * KVBLK);
;   SWAIT(); SWRITE(1, SO); __syncthreads();
	v_mfma_f32_32x32x16_bf16 v[32:47], v[72:75], v[98:101], v[32:47]
	s_nop 2
	v_max_f32_e32 v72, v17, v17
	v_max_f32_e32 v73, v16, v16
	v_max_f32_e32 v72, v73, v72
	v_max3_f32 v72, v72, v18, v19
	v_max3_f32 v72, v72, v20, v21
	v_max3_f32 v72, v72, v22, v23
	v_max3_f32 v72, v72, v24, v25
	v_max3_f32 v72, v72, v26, v27
	v_max3_f32 v72, v72, v28, v29
	v_max3_f32 v72, v72, v30, v31
	v_max3_f32 v72, v72, v32, v33
	v_max3_f32 v72, v72, v34, v35
	v_max3_f32 v72, v72, v36, v37
	v_max3_f32 v72, v72, v38, v39
	v_max3_f32 v72, v72, v40, v41
	v_max3_f32 v72, v72, v42, v43
	v_max3_f32 v72, v72, v44, v45
	v_max3_f32 v72, v72, v46, v47
	v_mov_b32_e32 v73, v72
	s_nop 1
	v_permlane32_swap_b32_e32 v72, v73
	v_max_f32_e32 v73, v73, v73
	v_max_f32_e32 v72, v72, v72
	v_max_f32_e32 v72, v72, v73
	v_add_f32_e32 v73, 0x7149f2ca, v72
	v_cmp_ge_f32_e32 vcc, s87, v73
	s_cmp_eq_u64 vcc, exec
	v_max_f32_e32 v56, 0xf149f2ca, v72
	s_cselect_b64 vcc, -1, 0
	v_cndmask_b32_e32 v170, v56, v217, vcc
	v_sub_f32_e32 v57, 0xf149f2ca, v56
	v_mul_f32_e32 v56, 0xbe0293ee, v170
	v_fmamk_f32 v16, v16, 0x3e0293ee, v56
	v_exp_f32_e32 v163, v16
	v_fmamk_f32 v16, v17, 0x3e0293ee, v56
	v_exp_f32_e32 v177, v16
	v_fmamk_f32 v16, v18, 0x3e0293ee, v56
	v_exp_f32_e32 v164, v16
	v_fmamk_f32 v16, v19, 0x3e0293ee, v56
	v_exp_f32_e32 v188, v16
	v_fmamk_f32 v16, v20, 0x3e0293ee, v56
	v_exp_f32_e32 v176, v16
	v_fmamk_f32 v16, v21, 0x3e0293ee, v56
	v_exp_f32_e32 v189, v16
	v_fmamk_f32 v16, v22, 0x3e0293ee, v56
	v_exp_f32_e32 v165, v16
	v_fmamk_f32 v16, v23, 0x3e0293ee, v56
	v_exp_f32_e32 v175, v16
	v_fmamk_f32 v16, v24, 0x3e0293ee, v56
	v_mul_f32_e32 v57, 0x3e0293ee, v57
	v_exp_f32_e32 v166, v16
	v_fmamk_f32 v16, v25, 0x3e0293ee, v56
	v_exp_f32_e32 v57, v57
	v_exp_f32_e32 v173, v16
	v_fmamk_f32 v16, v26, 0x3e0293ee, v56
	v_exp_f32_e32 v167, v16
	v_fmamk_f32 v16, v27, 0x3e0293ee, v56
	v_exp_f32_e32 v174, v16
	v_fmamk_f32 v16, v28, 0x3e0293ee, v56
	v_exp_f32_e32 v168, v16
	v_fmamk_f32 v16, v29, 0x3e0293ee, v56
	v_pk_fma_f32 v[146:147], v[46:47], s[10:11], v[56:57] op_sel_hi:[1,0,0]
	v_pk_fma_f32 v[152:153], v[44:45], s[10:11], v[56:57] op_sel_hi:[1,0,0]
	v_pk_fma_f32 v[156:157], v[42:43], s[10:11], v[56:57] op_sel_hi:[1,0,0]
	v_pk_fma_f32 v[148:149], v[40:41], s[10:11], v[56:57] op_sel_hi:[1,0,0]
	v_pk_fma_f32 v[150:151], v[38:39], s[10:11], v[56:57] op_sel_hi:[1,0,0]
	v_pk_fma_f32 v[154:155], v[36:37], s[10:11], v[56:57] op_sel_hi:[1,0,0]
	v_pk_fma_f32 v[158:159], v[34:35], s[10:11], v[56:57] op_sel_hi:[1,0,0]
	v_pk_fma_f32 v[160:161], v[32:33], s[10:11], v[56:57] op_sel_hi:[1,0,0]
	v_exp_f32_e32 v171, v16
	v_fmamk_f32 v16, v30, 0x3e0293ee, v56
	v_fmac_f32_e32 v56, 0x3e0293ee, v31
	v_exp_f32_e32 v169, v16
	v_exp_f32_e32 v172, v56
	v_mov_b64_e32 v[12:13], s[76:77]
	v_cndmask_b32_e64 v226, v57, 1.0, vcc
	s_add_i32 s34, 0, 0x4000
	v_mov_b64_e32 v[62:63], v[14:15]
	v_mov_b64_e32 v[46:47], v[14:15]
	v_mov_b64_e32 v[30:31], v[14:15]
	v_add_u32_e32 v203, s34, v77
	v_mov_b64_e32 v[60:61], v[12:13]
	v_mov_b64_e32 v[58:59], v[10:11]
	v_mov_b64_e32 v[56:57], v[8:9]
	v_mov_b64_e32 v[54:55], v[6:7]
	v_mov_b64_e32 v[52:53], v[4:5]
	v_mov_b64_e32 v[50:51], v[2:3]
	v_mov_b64_e32 v[48:49], v[0:1]
	v_mov_b64_e32 v[44:45], v[12:13]
	v_mov_b64_e32 v[42:43], v[10:11]
	v_mov_b64_e32 v[40:41], v[8:9]
	v_mov_b64_e32 v[38:39], v[6:7]
	v_mov_b64_e32 v[36:37], v[4:5]
	v_mov_b64_e32 v[34:35], v[2:3]
	v_mov_b64_e32 v[32:33], v[0:1]
	v_mov_b64_e32 v[28:29], v[12:13]
	v_mov_b64_e32 v[26:27], v[10:11]
	v_mov_b64_e32 v[24:25], v[8:9]
	v_mov_b64_e32 v[22:23], v[6:7]
	v_mov_b64_e32 v[20:21], v[4:5]
	v_mov_b64_e32 v[18:19], v[2:3]
	v_mov_b64_e32 v[16:17], v[0:1]
	s_waitcnt lgkmcnt(0)
	s_barrier
	s_add_i32 m0, s52, 0x0
	s_nop 0
	global_load_lds_dwordx4 v130, s[48:49]
	s_add_i32 m0, s52, 0x400
	s_nop 0
	global_load_lds_dwordx4 v131, s[48:49]
	s_add_u32 s48, s48, 0x18000
	s_addc_u32 s49, s49, 0
	s_nop 0
	s_mov_b32 s54, 0

; __device__ __forceinline__ unsigned xb_ld(unsigned* p)              { return __hip_atomic_load(p, __ATOMIC_RELAXED, __HIP_MEMORY_SCOPE_AGENT); }
; __device__ __forceinline__ void xcd_barrier_complete(unsigned* bar, unsigned x, unsigned& nloc, unsigned& nx) {
;     const unsigned G = gridDim.x * gridDim.y * gridDim.z;
;     unsigned sum, cnt, mine, sp = 0u;
;     for (;;) {
;         sum = 0u; cnt = 0u; mine = 0u;
; #pragma unroll
;         for (unsigned j = 0; j < 16; ++j) { const unsigned c = xb_ld(&bar[XB_XCNT(j)]); sum += c; cnt += (c > 0u) ? 1u : 0u; mine = (j == x) ? c : mine; }
;         if (sum == G) break;
;         __builtin_amdgcn_s_sleep(1);
;         if ((++sp & 255u) == 0u) { if (xb_ld(&bar[XB_TMO])) break; if (sp > XB_SPIN_CAP) { atomicAdd(&bar[XB_TMO], 1u); break; } }
;     }
;     nloc = mine > 0u ? mine : 1u; nx = cnt > 0u ? cnt : 1u;
; }
; __device__ __forceinline__ void xcd_barrier(const XcdBarrier& b) {
;     asm volatile("s_waitcnt vmcnt(0)" ::: "memory");
;     __syncthreads();
;     if (threadIdx.x == 0) {
;         unsigned* bar = b.bar;
;         __builtin_amdgcn_s_waitcnt(0);
;         unsigned nloc = b.st[0], nx = b.st[1];
;         if (nloc == 0u) { xcd_barrier_complete(bar, b.x, nloc, nx); b.st[0] = nloc; b.st[1] = nx; }
.LBB0_593:
	s_nop 0
	v_readlane_b32 s0, v255, 22
	v_readlane_b32 s4, v252, 12
	s_add_i32 s0, s0, 7
	v_readlane_b32 s5, v252, 13
	s_cmp_ge_i32 s0, s5
	v_readlane_b32 s6, v252, 14
	v_readlane_b32 s7, v252, 15
	s_cbranch_scc1 .LBB0_647
	s_waitcnt vmcnt(0)
	s_waitcnt vmcnt(0)
	s_barrier
	s_mov_b64 s[0:1], exec
	v_readlane_b32 s2, v252, 9
	v_readlane_b32 s3, v252, 10
	s_and_b64 s[2:3], s[0:1], s[2:3]
	s_mov_b64 exec, s[2:3]
	s_cbranch_execz .LBB0_646
	v_readlane_b32 s2, v255, 5
	s_waitcnt vmcnt(0) expcnt(0) lgkmcnt(0)
	s_nop 0
	v_mov_b32_e32 v0, s2
	ds_read_b32 v2, v0
	v_readlane_b32 s2, v255, 6
	s_waitcnt lgkmcnt(0)
	v_cmp_ne_u32_e32 vcc, 0, v2
	v_mov_b32_e32 v0, s2
	ds_read_b32 v0, v0
	s_cbranch_vccnz .LBB0_610
	v_readlane_b32 s4, v252, 2
	v_readlane_b32 s5, v252, 3
	s_load_dwordx2 s[2:3], s[4:5], 0x4
	s_waitcnt lgkmcnt(0)
	s_mul_i32 s2, s2, s97
	s_mul_i32 s2, s2, s3
	s_mov_b32 s3, 1
	s_branch .LBB0_598
